# stack7 + non-temporal hint on the P1 x row loads and the final output stores
# baseline (speedup 1.0000x reference)
; #define LAS __attribute__((address_space(3)))
; __device__ __forceinline__ unsigned cvt_pk_bf16(float lo, float hi) { const f32x2 v = {lo, hi}; return __builtin_bit_cast(unsigned, __builtin_convertvector(v, bf16x2_t)); }
; __device__ __forceinline__ void p1_norm1(const Params& P, LAS unsigned char* lds, int tid, int blk, int G) {
;     ...
;         for (int rr = 0; rr < 8; ++rr) {
;             const int row = rb * 64 + wave * 8 + rr;
;             if (rr < 7) { const float* xn = P.in[0] + (size_t)(row + 1) * DM;
; #pragma unroll
;                 for (int i = 0; i < 8; ++i) vn[i] = *(const f32x4*)(xn + (i * 64 + lane) * 4); }
;             float ss = 0.f;
; #pragma unroll
;             for (int i = 0; i < 8; ++i) ss += v[i][0] * v[i][0] + v[i][1] * v[i][1] + v[i][2] * v[i][2] + v[i][3] * v[i][3];
;             ss = wave_sum(ss);
;             const float r = rsqrtf(ss * (1.0f / 2048.0f) + 1e-6f);
; #pragma unroll
;             for (int i = 0; i < 8; ++i) {
;                 const int k = (i * 64 + lane) * 4;
;                 const f32x4 g4 = *(const LAS f32x4*)(gm + k), s4 = *(const LAS f32x4*)(sh + k);
;                 const f32x4 o = v[i] * r * g4 + s4;
;                 u32x2 w; w.x = cvt_pk_bf16(o[0], o[1]); w.y = cvt_pk_bf16(o[2], o[3]);
;                 __hip_atomic_store((unsigned long long*)(H + (size_t)row * DM + k), __builtin_bit_cast(unsigned long long, w), __ATOMIC_RELAXED, __HIP_MEMORY_SCOPE_AGENT);
;             }
.LBB0_173:
	s_waitcnt vmcnt(7)
	v_mul_f32_e32 v79, v35, v35
	s_waitcnt vmcnt(6)
	v_mul_f32_e32 v87, v39, v39
	s_waitcnt vmcnt(5)
	v_mul_f32_e32 v120, v43, v43
	v_fmac_f32_e32 v79, v34, v34
	v_fmac_f32_e32 v87, v38, v38
	s_waitcnt vmcnt(4)
	v_mul_f32_e32 v121, v47, v47
	s_waitcnt vmcnt(2)
	v_pk_mul_f32 v[24:25], v[54:55], v[54:55]
	v_pk_mul_f32 v[98:99], v[50:51], v[50:51]
	v_fmac_f32_e32 v120, v42, v42
	v_fmac_f32_e32 v79, v36, v36
	v_fmac_f32_e32 v87, v40, v40
	v_pk_mul_f32 v[22:23], v[56:57], v[56:57]
	v_pk_mul_f32 v[94:95], v[52:53], v[52:53]
	v_mov_b32_e32 v110, v24
	v_mov_b32_e32 v111, v98
	v_mov_b32_e32 v98, v25
	v_fmac_f32_e32 v121, v46, v46
	v_fmac_f32_e32 v120, v44, v44
	v_fmac_f32_e32 v79, v37, v37
	v_fmac_f32_e32 v87, v41, v41
	s_waitcnt vmcnt(0)
	v_pk_mul_f32 v[20:21], v[62:63], v[62:63]
	v_pk_mul_f32 v[96:97], v[58:59], v[58:59]
	v_mov_b32_e32 v112, v22
	v_mov_b32_e32 v113, v94
	v_pk_add_f32 v[98:99], v[110:111], v[98:99]
	v_fmac_f32_e32 v121, v48, v48
	v_fmac_f32_e32 v120, v45, v45
	v_add_f32_e32 v79, v79, v87
	v_pk_mul_f32 v[18:19], v[64:65], v[64:65]
	v_pk_mul_f32 v[92:93], v[60:61], v[60:61]
	v_mov_b32_e32 v94, v23
	v_mov_b32_e32 v114, v20
	v_mov_b32_e32 v115, v96
	v_mov_b32_e32 v96, v21
	v_pk_add_f32 v[98:99], v[112:113], v[98:99]
	v_fmac_f32_e32 v121, v49, v49
	v_add_f32_e32 v79, v120, v79
	v_mov_b32_e32 v116, v18
	v_mov_b32_e32 v117, v92
	v_pk_add_f32 v[96:97], v[114:115], v[96:97]
	v_pk_add_f32 v[94:95], v[94:95], v[98:99]
	v_add_f32_e32 v79, v121, v79
	v_mov_b32_e32 v92, v19
	v_pk_add_f32 v[96:97], v[116:117], v[96:97]
	v_add_f32_e32 v79, v95, v79
	v_pk_add_f32 v[92:93], v[92:93], v[96:97]
	v_add_f32_e32 v79, v94, v79
	v_add_f32_e32 v79, v93, v79
	v_add_f32_e32 v79, v92, v79
	ds_bpermute_b32 v87, v100, v79
	v_add_co_u32_e32 v30, vcc, s28, v90
	v_lshl_add_u64 v[26:27], v[88:89], 0, s[8:9]
	s_nop 0
	v_addc_co_u32_e32 v31, vcc, 0, v91, vcc
	s_waitcnt lgkmcnt(0)
	v_add_f32_e32 v79, v79, v87
	ds_bpermute_b32 v87, v101, v79
	v_add_co_u32_e32 v118, vcc, s30, v26
	global_load_dwordx4 v[6:9], v[90:91], off offset:3072 nt
	global_load_dwordx4 v[10:13], v[90:91], off offset:2048 nt
	global_load_dwordx4 v[14:17], v[90:91], off offset:1024 nt
	global_load_dwordx4 v[2:5], v[90:91], off nt
	ds_read_b128 v[66:69], v106
	ds_read_b128 v[70:73], v106 offset:8192
	s_waitcnt lgkmcnt(2)
	v_add_f32_e32 v79, v79, v87
	ds_bpermute_b32 v87, v102, v79
	v_addc_co_u32_e32 v119, vcc, 0, v27, vcc
	global_load_dwordx4 v[18:21], v[30:31], off offset:3072 nt
	global_load_dwordx4 v[22:25], v[30:31], off offset:2048 nt
	global_load_dwordx4 v[26:29], v[30:31], off offset:1024 nt
	s_nop 0
	global_load_dwordx4 v[30:33], v[30:31], off nt
	s_waitcnt lgkmcnt(0)
	v_add_f32_e32 v79, v79, v87
	ds_bpermute_b32 v87, v103, v79
	s_add_u32 s8, s8, 0x1000
	s_addc_u32 s9, s9, 0
	v_lshl_add_u64 v[90:91], v[90:91], 0, s[4:5]
	s_cmpk_eq_i32 s8, 0x7000
	s_waitcnt lgkmcnt(0)
	v_add_f32_e32 v79, v79, v87
	ds_bpermute_b32 v87, v104, v79
	s_waitcnt lgkmcnt(0)
	v_add_f32_e32 v79, v79, v87
	ds_bpermute_b32 v87, v105, v79
	s_waitcnt lgkmcnt(0)
	v_add_f32_e32 v79, v79, v87
	v_fmamk_f32 v79, v79, 0x3a000000, v109
	v_mul_f32_e32 v87, 0x4b800000, v79
	v_cmp_gt_f32_e32 vcc, s29, v79
	s_nop 1
	v_cndmask_b32_e32 v79, v79, v87, vcc
	v_rsq_f32_e32 v79, v79
	s_nop 0
	v_mul_f32_e32 v87, 0x45800000, v79
	v_cndmask_b32_e32 v92, v79, v87, vcc
	v_pk_mul_f32 v[34:35], v[34:35], v[92:93] op_sel_hi:[1,0]
	v_pk_mul_f32 v[36:37], v[36:37], v[92:93] op_sel_hi:[1,0]
	v_pk_fma_f32 v[34:35], v[66:67], v[34:35], v[70:71]
	v_pk_fma_f32 v[36:37], v[68:69], v[36:37], v[72:73]
	v_cvt_pk_bf16_f32 v34, v34, v35
	v_cvt_pk_bf16_f32 v35, v36, v37
	global_store_dwordx2 v[118:119], v[34:35], off sc1
	v_pk_mul_f32 v[94:95], v[38:39], v[92:93] op_sel_hi:[1,0]
	v_pk_mul_f32 v[96:97], v[40:41], v[92:93] op_sel_hi:[1,0]
	ds_read_b128 v[34:37], v106 offset:1024
	ds_read_b128 v[38:41], v106 offset:9216
	v_pk_mul_f32 v[42:43], v[42:43], v[92:93] op_sel_hi:[1,0]
	v_pk_mul_f32 v[44:45], v[44:45], v[92:93] op_sel_hi:[1,0]
	v_pk_mul_f32 v[112:113], v[50:51], v[92:93] op_sel_hi:[1,0]
	v_pk_mul_f32 v[114:115], v[52:53], v[92:93] op_sel_hi:[1,0]
	s_waitcnt lgkmcnt(0)
	v_pk_fma_f32 v[36:37], v[36:37], v[96:97], v[40:41]
	v_pk_fma_f32 v[34:35], v[34:35], v[94:95], v[38:39]
	v_pk_mul_f32 v[116:117], v[54:55], v[92:93] op_sel_hi:[1,0]
	v_cvt_pk_bf16_f32 v34, v34, v35
	v_cvt_pk_bf16_f32 v35, v36, v37
	global_store_dwordx2 v[118:119], v[34:35], off offset:512 sc1
	ds_read_b128 v[34:37], v106 offset:2048
	ds_read_b128 v[38:41], v106 offset:10240
	v_pk_mul_f32 v[120:121], v[56:57], v[92:93] op_sel_hi:[1,0]
	v_pk_mul_f32 v[98:99], v[46:47], v[92:93] op_sel_hi:[1,0]
	v_pk_mul_f32 v[110:111], v[48:49], v[92:93] op_sel_hi:[1,0]
	v_pk_mul_f32 v[122:123], v[58:59], v[92:93] op_sel_hi:[1,0]
	s_waitcnt lgkmcnt(0)
	v_pk_fma_f32 v[36:37], v[36:37], v[44:45], v[40:41]
	v_pk_fma_f32 v[34:35], v[34:35], v[42:43], v[38:39]
	v_pk_mul_f32 v[124:125], v[60:61], v[92:93] op_sel_hi:[1,0]
	v_cvt_pk_bf16_f32 v34, v34, v35
	v_cvt_pk_bf16_f32 v35, v36, v37
	global_store_dwordx2 v[118:119], v[34:35], off offset:1024 sc1
	ds_read_b128 v[50:53], v106 offset:3072
	ds_read_b128 v[54:57], v106 offset:11264
	v_pk_mul_f32 v[126:127], v[62:63], v[92:93] op_sel_hi:[1,0]
	v_pk_mul_f32 v[92:93], v[64:65], v[92:93] op_sel_hi:[1,0]
	s_waitcnt lgkmcnt(0)
	v_pk_fma_f32 v[64:65], v[52:53], v[110:111], v[56:57]
	v_pk_fma_f32 v[66:67], v[50:51], v[98:99], v[54:55]
	s_waitcnt vmcnt(10)
	v_mov_b32_e32 v46, v6
	v_cvt_pk_bf16_f32 v66, v66, v67
	v_cvt_pk_bf16_f32 v67, v64, v65
	global_store_dwordx2 v[118:119], v[66:67], off offset:1536 sc1
	ds_read_b128 v[64:67], v106 offset:4096
	ds_read_b128 v[68:71], v106 offset:12288
	s_waitcnt vmcnt(8)
; #define LAS __attribute__((address_space(3)))
; __device__ __forceinline__ unsigned cvt_pk_bf16(float lo, float hi) { const f32x2 v = {lo, hi}; return __builtin_bit_cast(unsigned, __builtin_convertvector(v, bf16x2_t)); }
; __device__ __forceinline__ void p1_norm1(const Params& P, LAS unsigned char* lds, int tid, int blk, int G) {
;     ...
;             for (int i = 0; i < 8; ++i) {
;                 const int k = (i * 64 + lane) * 4;
;                 const f32x4 g4 = *(const LAS f32x4*)(gm + k), s4 = *(const LAS f32x4*)(sh + k);
;                 const f32x4 o = v[i] * r * g4 + s4;
;                 u32x2 w; w.x = cvt_pk_bf16(o[0], o[1]); w.y = cvt_pk_bf16(o[2], o[3]);
;                 __hip_atomic_store((unsigned long long*)(H + (size_t)row * DM + k), __builtin_bit_cast(unsigned long long, w), __ATOMIC_RELAXED, __HIP_MEMORY_SCOPE_AGENT);
;             }
; #pragma unroll
;             for (int i = 0; i < 8; ++i) v[i] = vn[i];
;         }
	v_mov_b32_e32 v34, v2
	v_mov_b32_e32 v35, v3
	v_mov_b32_e32 v36, v4
	v_mov_b32_e32 v37, v5
	s_waitcnt lgkmcnt(0)
	v_pk_fma_f32 v[66:67], v[66:67], v[114:115], v[70:71]
	v_pk_fma_f32 v[64:65], v[64:65], v[112:113], v[68:69]
	v_mov_b32_e32 v38, v14
	v_cvt_pk_bf16_f32 v64, v64, v65
	v_cvt_pk_bf16_f32 v65, v66, v67
	global_store_dwordx2 v[118:119], v[64:65], off offset:2048 sc1
	ds_read_b128 v[64:67], v106 offset:5120
	ds_read_b128 v[68:71], v106 offset:13312
	v_mov_b32_e32 v39, v15
	v_mov_b32_e32 v40, v16
	v_mov_b32_e32 v41, v17
	v_mov_b32_e32 v42, v10
	s_waitcnt lgkmcnt(0)
	v_pk_fma_f32 v[66:67], v[120:121], v[66:67], v[70:71]
	v_pk_fma_f32 v[64:65], v[116:117], v[64:65], v[68:69]
	v_mov_b32_e32 v43, v11
	v_cvt_pk_bf16_f32 v64, v64, v65
	v_cvt_pk_bf16_f32 v65, v66, v67
	global_store_dwordx2 v[118:119], v[64:65], off offset:2560 sc1
	ds_read_b128 v[64:67], v106 offset:6144
	ds_read_b128 v[68:71], v106 offset:14336
	v_mov_b32_e32 v44, v12
	v_mov_b32_e32 v45, v13
	v_mov_b32_e32 v47, v7
	v_mov_b32_e32 v48, v8
	s_waitcnt lgkmcnt(0)
	v_pk_fma_f32 v[66:67], v[124:125], v[66:67], v[70:71]
	v_pk_fma_f32 v[64:65], v[122:123], v[64:65], v[68:69]
	v_mov_b32_e32 v49, v9
	v_cvt_pk_bf16_f32 v64, v64, v65
	v_cvt_pk_bf16_f32 v65, v66, v67
	global_store_dwordx2 v[118:119], v[64:65], off offset:3072 sc1
	ds_read_b128 v[66:69], v106 offset:7168
	ds_read_b128 v[70:73], v106 offset:15360
	s_waitcnt vmcnt(7)
	v_mov_b32_e32 v50, v30
	v_mov_b32_e32 v51, v31
	v_mov_b32_e32 v52, v32
	v_mov_b32_e32 v53, v33
	s_waitcnt lgkmcnt(0)
	v_pk_fma_f32 v[68:69], v[92:93], v[68:69], v[72:73]
	v_pk_fma_f32 v[66:67], v[126:127], v[66:67], v[70:71]
	v_mov_b32_e32 v54, v26
	v_mov_b32_e32 v55, v27
	v_mov_b32_e32 v56, v28
	v_mov_b32_e32 v57, v29
	v_mov_b32_e32 v58, v22
	v_mov_b32_e32 v59, v23
	v_mov_b32_e32 v60, v24
	v_mov_b32_e32 v61, v25
	v_mov_b32_e32 v62, v18
	v_mov_b32_e32 v63, v19
	v_mov_b32_e32 v64, v20
	v_mov_b32_e32 v65, v21
	v_cvt_pk_bf16_f32 v66, v66, v67
	v_cvt_pk_bf16_f32 v67, v68, v69
	global_store_dwordx2 v[118:119], v[66:67], off offset:3584 sc1
	s_cbranch_scc0 .LBB0_173
; #define LAS __attribute__((address_space(3)))
; __device__ __forceinline__ unsigned cvt_pk_bf16(float lo, float hi) { const f32x2 v = {lo, hi}; return __builtin_bit_cast(unsigned, __builtin_convertvector(v, bf16x2_t)); }
; __device__ __forceinline__ void p1_norm1(const Params& P, LAS unsigned char* lds, int tid, int blk, int G) {
;     ...
;         for (int rr = 0; rr < 8; ++rr) {
;             const int row = rb * 64 + wave * 8 + rr;
;             if (rr < 7) { const float* xn = P.in[0] + (size_t)(row + 1) * DM;
; #pragma unroll
;                 for (int i = 0; i < 8; ++i) vn[i] = *(const f32x4*)(xn + (i * 64 + lane) * 4); }
;             float ss = 0.f;
; #pragma unroll
;             for (int i = 0; i < 8; ++i) ss += v[i][0] * v[i][0] + v[i][1] * v[i][1] + v[i][2] * v[i][2] + v[i][3] * v[i][3];
;             ss = wave_sum(ss);
;             const float r = rsqrtf(ss * (1.0f / 2048.0f) + 1e-6f);
; #pragma unroll
;             for (int i = 0; i < 8; ++i) {
;                 const int k = (i * 64 + lane) * 4;
;                 const f32x4 g4 = *(const LAS f32x4*)(gm + k), s4 = *(const LAS f32x4*)(sh + k);
;                 const f32x4 o = v[i] * r * g4 + s4;
;                 u32x2 w; w.x = cvt_pk_bf16(o[0], o[1]); w.y = cvt_pk_bf16(o[2], o[3]);
;                 __hip_atomic_store((unsigned long long*)(H + (size_t)row * DM + k), __builtin_bit_cast(unsigned long long, w), __ATOMIC_RELAXED, __HIP_MEMORY_SCOPE_AGENT);
;             }
; #pragma unroll
;             for (int i = 0; i < 8; ++i) v[i] = vn[i];
;         }
;         __syncthreads();
	v_mul_f32_e32 v34, v3, v3
	v_mul_f32_e32 v35, v15, v15
	v_fmac_f32_e32 v34, v2, v2
	v_fmac_f32_e32 v35, v14, v14
	v_fmac_f32_e32 v34, v4, v4
	v_fmac_f32_e32 v35, v16, v16
	v_fmac_f32_e32 v34, v5, v5
	v_fmac_f32_e32 v35, v17, v17
	v_add_f32_e32 v34, v35, v34
	v_mul_f32_e32 v35, v11, v11
	v_fmac_f32_e32 v35, v10, v10
	v_fmac_f32_e32 v35, v12, v12
	v_fmac_f32_e32 v35, v13, v13
	v_add_f32_e32 v34, v35, v34
	v_mul_f32_e32 v35, v7, v7
	v_fmac_f32_e32 v35, v6, v6
	v_fmac_f32_e32 v35, v8, v8
	v_fmac_f32_e32 v35, v9, v9
	v_mov_b32_e32 v36, v27
	v_mov_b32_e32 v37, v31
	v_add_f32_e32 v38, v35, v34
	v_mov_b32_e32 v34, v26
	v_mov_b32_e32 v35, v30
	v_pk_mul_f32 v[36:37], v[36:37], v[36:37]
	v_ashrrev_i32_e32 v87, 31, v86
	v_pk_fma_f32 v[34:35], v[34:35], v[34:35], v[36:37]
	v_mov_b32_e32 v36, v28
	v_mov_b32_e32 v37, v32
	v_pk_fma_f32 v[34:35], v[36:37], v[36:37], v[34:35]
	v_mov_b32_e32 v36, v29
	v_mov_b32_e32 v37, v33
	v_pk_fma_f32 v[34:35], v[36:37], v[36:37], v[34:35]
	v_mov_b32_e32 v36, v19
	v_add_f32_e32 v35, v35, v38
	v_mov_b32_e32 v37, v23
	v_add_f32_e32 v38, v34, v35
	v_mov_b32_e32 v34, v18
	v_mov_b32_e32 v35, v22
	v_pk_mul_f32 v[36:37], v[36:37], v[36:37]
	v_lshlrev_b64 v[44:45], 12, v[86:87]
	v_pk_fma_f32 v[34:35], v[34:35], v[34:35], v[36:37]
	v_mov_b32_e32 v36, v20
	v_mov_b32_e32 v37, v24
	v_pk_fma_f32 v[34:35], v[36:37], v[36:37], v[34:35]
	v_mov_b32_e32 v36, v21
	v_mov_b32_e32 v37, v25
	v_pk_fma_f32 v[34:35], v[36:37], v[36:37], v[34:35]
	v_lshl_add_u64 v[44:45], v[80:81], 0, v[44:45]
	v_add_f32_e32 v35, v35, v38
	v_add_f32_e32 v34, v34, v35
	ds_bpermute_b32 v35, v100, v34
	s_add_i32 s34, s34, s33
	s_cmpk_gt_i32 s34, 0xff
	s_waitcnt lgkmcnt(0)
	v_add_f32_e32 v34, v34, v35
	ds_bpermute_b32 v35, v101, v34
	s_waitcnt lgkmcnt(0)
	v_add_f32_e32 v34, v34, v35
	ds_bpermute_b32 v35, v102, v34
	s_waitcnt lgkmcnt(0)
	v_add_f32_e32 v34, v34, v35
	ds_bpermute_b32 v35, v103, v34
	s_waitcnt lgkmcnt(0)
	v_add_f32_e32 v34, v34, v35
	ds_bpermute_b32 v35, v104, v34
	s_waitcnt lgkmcnt(0)
	v_add_f32_e32 v34, v34, v35
	ds_bpermute_b32 v35, v105, v34
	s_waitcnt lgkmcnt(0)
	v_add_f32_e32 v34, v34, v35
	v_fmamk_f32 v34, v34, 0x3a000000, v109
	v_mul_f32_e32 v35, 0x4b800000, v34
	v_cmp_gt_f32_e32 vcc, s29, v34
	s_nop 1
	v_cndmask_b32_e32 v34, v34, v35, vcc
	v_rsq_f32_e32 v34, v34
	s_nop 0
	v_mul_f32_e32 v35, 0x45800000, v34
	v_cndmask_b32_e32 v42, v34, v35, vcc
	ds_read_b128 v[34:37], v106
	ds_read_b128 v[38:41], v106 offset:8192
	v_pk_mul_f32 v[46:47], v[2:3], v[42:43] op_sel_hi:[1,0]
	v_pk_mul_f32 v[48:49], v[4:5], v[42:43] op_sel_hi:[1,0]
	s_waitcnt lgkmcnt(0)
	v_pk_fma_f32 v[34:35], v[34:35], v[46:47], v[38:39]
	v_pk_fma_f32 v[36:37], v[36:37], v[48:49], v[40:41]
	v_cvt_pk_bf16_f32 v34, v34, v35
	v_cvt_pk_bf16_f32 v35, v36, v37
	v_add_co_u32_e32 v36, vcc, s31, v44
	v_pk_mul_f32 v[46:47], v[14:15], v[42:43] op_sel_hi:[1,0]
	s_nop 0
	v_addc_co_u32_e32 v37, vcc, 0, v45, vcc
	global_store_dwordx2 v[36:37], v[34:35], off sc1
	ds_read_b128 v[34:37], v106 offset:1024
	ds_read_b128 v[38:41], v106 offset:9216
	v_pk_mul_f32 v[48:49], v[16:17], v[42:43] op_sel_hi:[1,0]
	v_lshl_add_u64 v[44:45], v[44:45], 0, s[6:7]
	s_waitcnt lgkmcnt(0)
	v_pk_fma_f32 v[36:37], v[36:37], v[48:49], v[40:41]
	v_pk_fma_f32 v[34:35], v[34:35], v[46:47], v[38:39]
	v_pk_mul_f32 v[46:47], v[10:11], v[42:43] op_sel_hi:[1,0]
	v_cvt_pk_bf16_f32 v34, v34, v35
	v_cvt_pk_bf16_f32 v35, v36, v37
	global_store_dwordx2 v[44:45], v[34:35], off offset:512 sc1
	ds_read_b128 v[34:37], v106 offset:2048
	ds_read_b128 v[38:41], v106 offset:10240
	v_pk_mul_f32 v[48:49], v[12:13], v[42:43] op_sel_hi:[1,0]
	s_waitcnt lgkmcnt(0)
	v_pk_fma_f32 v[34:35], v[34:35], v[46:47], v[38:39]
	v_pk_fma_f32 v[36:37], v[36:37], v[48:49], v[40:41]
	v_cvt_pk_bf16_f32 v34, v34, v35
	v_cvt_pk_bf16_f32 v35, v36, v37
	global_store_dwordx2 v[44:45], v[34:35], off offset:1024 sc1
	ds_read_b128 v[34:37], v106 offset:3072
	ds_read_b128 v[38:41], v106 offset:11264
	v_pk_mul_f32 v[46:47], v[6:7], v[42:43] op_sel_hi:[1,0]
	v_pk_mul_f32 v[48:49], v[8:9], v[42:43] op_sel_hi:[1,0]
	s_waitcnt lgkmcnt(0)
	v_pk_fma_f32 v[34:35], v[34:35], v[46:47], v[38:39]
	v_pk_fma_f32 v[36:37], v[36:37], v[48:49], v[40:41]
	v_cvt_pk_bf16_f32 v34, v34, v35
	v_cvt_pk_bf16_f32 v35, v36, v37
	global_store_dwordx2 v[44:45], v[34:35], off offset:1536 sc1
	ds_read_b128 v[34:37], v106 offset:4096
	ds_read_b128 v[38:41], v106 offset:12288
	v_pk_mul_f32 v[46:47], v[30:31], v[42:43] op_sel_hi:[1,0]
	v_pk_mul_f32 v[48:49], v[32:33], v[42:43] op_sel_hi:[1,0]
	s_waitcnt lgkmcnt(0)
	v_pk_fma_f32 v[34:35], v[46:47], v[34:35], v[38:39]
	v_pk_fma_f32 v[36:37], v[48:49], v[36:37], v[40:41]
	v_cvt_pk_bf16_f32 v34, v34, v35
	v_cvt_pk_bf16_f32 v35, v36, v37
	global_store_dwordx2 v[44:45], v[34:35], off offset:2048 sc1
	ds_read_b128 v[34:37], v106 offset:5120
	ds_read_b128 v[38:41], v106 offset:13312
	v_pk_mul_f32 v[46:47], v[26:27], v[42:43] op_sel_hi:[1,0]
	v_pk_mul_f32 v[48:49], v[28:29], v[42:43] op_sel_hi:[1,0]
	s_waitcnt lgkmcnt(0)
	v_pk_fma_f32 v[34:35], v[46:47], v[34:35], v[38:39]
	v_pk_fma_f32 v[36:37], v[48:49], v[36:37], v[40:41]
	v_cvt_pk_bf16_f32 v34, v34, v35
	v_cvt_pk_bf16_f32 v35, v36, v37
	global_store_dwordx2 v[44:45], v[34:35], off offset:2560 sc1
	ds_read_b128 v[34:37], v106 offset:6144
	ds_read_b128 v[38:41], v106 offset:14336
	v_pk_mul_f32 v[46:47], v[22:23], v[42:43] op_sel_hi:[1,0]
	v_pk_mul_f32 v[48:49], v[24:25], v[42:43] op_sel_hi:[1,0]
	s_waitcnt lgkmcnt(0)
	v_pk_fma_f32 v[34:35], v[46:47], v[34:35], v[38:39]
	v_pk_fma_f32 v[36:37], v[48:49], v[36:37], v[40:41]
	v_cvt_pk_bf16_f32 v34, v34, v35
	v_cvt_pk_bf16_f32 v35, v36, v37
	global_store_dwordx2 v[44:45], v[34:35], off offset:3072 sc1
	ds_read_b128 v[34:37], v106 offset:7168
	ds_read_b128 v[38:41], v106 offset:15360
	v_pk_mul_f32 v[46:47], v[18:19], v[42:43] op_sel_hi:[1,0]
	v_pk_mul_f32 v[42:43], v[20:21], v[42:43] op_sel_hi:[1,0]
	s_waitcnt lgkmcnt(0)
	v_pk_fma_f32 v[34:35], v[46:47], v[34:35], v[38:39]
	v_pk_fma_f32 v[36:37], v[42:43], v[36:37], v[40:41]
	v_cvt_pk_bf16_f32 v34, v34, v35
	v_cvt_pk_bf16_f32 v35, v36, v37
	global_store_dwordx2 v[44:45], v[34:35], off offset:3584 sc1
	s_barrier
	s_cbranch_scc0 .LBB0_166

; __device__ __forceinline__ float bf_lo(unsigned w) { return __uint_as_float(w << 16); }
; __device__ __forceinline__ float bf_hi(unsigned w) { return __uint_as_float(w & 0xffff0000u); }
; __device__ __forceinline__ void p9_final(const Params& P, int tid, int blk, int G) {
;     ...
;         f32x4 v[8]; float ss = 0.f;
; #pragma unroll
;         for (int i = 0; i < 8; ++i) {
;             const int k = (i * 64 + lane) * 4;
;             const f32x4 xv = {bf_lo(xw[i].x), bf_hi(xw[i].x), bf_lo(xw[i].y), bf_hi(xw[i].y)};
;             const f32x4 gt = *(const f32x4*)(mod + (size_t)b * NMOD + 5 * DM + k) * (1.0f / Y2_SCALE);
;             const f32x2 a0 = __builtin_amdgcn_cvt_pk_f32_fp8((int)ya[i], false), a1 = __builtin_amdgcn_cvt_pk_f32_fp8((int)ya[i], true);
;             const f32x2 b0 = __builtin_amdgcn_cvt_pk_f32_fp8((int)yb[i], false), b1 = __builtin_amdgcn_cvt_pk_f32_fp8((int)yb[i], true);
;             const f32x4 y = {a0[0] + b0[0], a0[1] + b0[1], a1[0] + b1[0], a1[1] + b1[1]};
;             v[i] = xv + gt * y;
;             ss += v[i][0] * v[i][0] + v[i][1] * v[i][1] + v[i][2] * v[i][2] + v[i][3] * v[i][3];
;         }
.LBB0_1459:
	s_or_b64 exec, exec, s[14:15]
	v_ashrrev_i32_e32 v43, 11, v88
	v_mul_hi_i32_i24_e32 v89, 0xc000, v43
	v_mul_i32_i24_e32 v88, 0xc000, v43
	v_lshl_add_u64 v[88:89], s[36:37], 0, v[88:89]
	v_lshl_add_u64 v[88:89], v[88:89], 0, s[10:11]
	v_mov_b32_e32 v43, v35
	v_mov_b32_e32 v45, v35
	v_mov_b32_e32 v47, v35
	v_lshl_add_u64 v[126:127], v[88:89], 0, v[34:35]
	v_lshl_add_u64 v[130:131], v[88:89], 0, v[42:43]
	v_lshl_add_u64 v[134:135], v[88:89], 0, v[44:45]
	v_lshl_add_u64 v[138:139], v[88:89], 0, v[46:47]
	global_load_dwordx4 v[126:129], v[126:127], off
	s_nop 0
	global_load_dwordx4 v[130:133], v[130:131], off
	s_waitcnt vmcnt(17)
	v_cvt_pk_f32_fp8_e32 v[142:143], v49
	global_load_dwordx4 v[134:137], v[134:135], off
	v_cvt_pk_f32_fp8_sdwa v[144:145], v49 src0_sel:WORD_1
	global_load_dwordx4 v[138:141], v[138:139], off
	v_mov_b32_e32 v49, v35
	v_lshlrev_b32_e32 v154, 16, v84
	v_and_b32_e32 v155, 0xffff0000, v84
	v_lshlrev_b32_e32 v156, 16, v85
	v_and_b32_e32 v157, 0xffff0000, v85
	v_lshl_add_u64 v[84:85], v[88:89], 0, v[48:49]
	v_lshlrev_b32_e32 v146, 16, v86
	v_and_b32_e32 v147, 0xffff0000, v86
	v_lshlrev_b32_e32 v148, 16, v87
	v_and_b32_e32 v149, 0xffff0000, v87
	global_load_dwordx4 v[84:87], v[84:85], off
	v_lshlrev_b32_e32 v166, 16, v82
	v_and_b32_e32 v167, 0xffff0000, v82
	v_lshlrev_b32_e32 v168, 16, v83
	v_and_b32_e32 v169, 0xffff0000, v83
	s_waitcnt vmcnt(18)
	v_cvt_pk_f32_fp8_e32 v[82:83], v51
	v_cvt_pk_f32_fp8_sdwa v[170:171], v51 src0_sel:WORD_1
	v_mov_b32_e32 v51, v35
	s_waitcnt vmcnt(11)
	v_cvt_pk_f32_fp8_e32 v[162:163], v123
	v_cvt_pk_f32_fp8_sdwa v[164:165], v123 src0_sel:WORD_1
	s_waitcnt vmcnt(10)
	v_cvt_pk_f32_fp8_e32 v[172:173], v122
	v_cvt_pk_f32_fp8_sdwa v[174:175], v122 src0_sel:WORD_1
	v_lshl_add_u64 v[122:123], v[88:89], 0, v[50:51]
	v_cvt_pk_f32_fp8_e32 v[150:151], v124
	v_cvt_pk_f32_fp8_sdwa v[152:153], v124 src0_sel:WORD_1
	global_load_dwordx4 v[122:125], v[122:123], off
	v_cvt_pk_f32_fp8_e32 v[158:159], v121
	v_cvt_pk_f32_fp8_e32 v[180:181], v53
	v_cvt_pk_f32_fp8_sdwa v[182:183], v53 src0_sel:WORD_1
	v_mov_b32_e32 v53, v35
	v_lshlrev_b32_e32 v176, 16, v80
	v_and_b32_e32 v177, 0xffff0000, v80
	v_lshlrev_b32_e32 v178, 16, v81
	v_and_b32_e32 v179, 0xffff0000, v81
	s_waitcnt vmcnt(10)
	v_cvt_pk_f32_fp8_e32 v[184:185], v55
	v_cvt_pk_f32_fp8_sdwa v[186:187], v55 src0_sel:WORD_1
	v_mov_b32_e32 v55, v35
	v_lshl_add_u64 v[80:81], v[88:89], 0, v[52:53]
	v_pk_add_f32 v[150:151], v[142:143], v[150:151]
	v_pk_add_f32 v[152:153], v[144:145], v[152:153]
	v_pk_add_f32 v[158:159], v[158:159], v[162:163]
	v_pk_add_f32 v[162:163], v[82:83], v[172:173]
	v_lshl_add_u64 v[88:89], v[88:89], 0, v[54:55]
	global_load_dwordx4 v[80:83], v[80:81], off
	s_nop 0
	global_load_dwordx4 v[142:145], v[88:89], off
	v_cvt_pk_f32_fp8_sdwa v[160:161], v121 src0_sel:WORD_1
	s_and_b64 s[14:15], exec, vcc
	s_or_b64 s[8:9], s[14:15], s[8:9]
	v_add_u32_e32 v38, s16, v38
	v_pk_add_f32 v[160:161], v[160:161], v[164:165]
	v_pk_add_f32 v[164:165], v[170:171], v[174:175]
	v_lshl_add_u64 v[40:41], v[40:41], 0, s[6:7]
	v_mov_b32_e32 v53, v100
	v_mov_b32_e32 v51, v101
	v_mov_b32_e32 v121, v102
	v_mov_b32_e32 v49, v103
	v_mov_b32_e32 v55, v109
	s_waitcnt vmcnt(7)
	v_pk_mul_f32 v[126:127], v[126:127], s[12:13] op_sel_hi:[1,0]
	v_pk_mul_f32 v[88:89], v[128:129], s[12:13] op_sel_hi:[1,0]
	s_waitcnt vmcnt(6)
	v_pk_mul_f32 v[128:129], v[132:133], s[12:13] op_sel_hi:[1,0]
	s_waitcnt vmcnt(5)
	v_pk_mul_f32 v[132:133], v[136:137], s[12:13] op_sel_hi:[1,0]
	v_pk_fma_f32 v[126:127], v[126:127], v[150:151], v[146:147]
	s_waitcnt vmcnt(4)
	v_pk_mul_f32 v[136:137], v[140:141], s[12:13] op_sel_hi:[1,0]
	v_pk_add_f32 v[146:147], v[182:183], v[186:187]
	v_cvt_pk_f32_fp8_e32 v[150:151], v119
	v_pk_fma_f32 v[136:137], v[136:137], v[146:147], v[178:179]
	v_cvt_pk_f32_fp8_e32 v[146:147], v117
	v_pk_mul_f32 v[138:139], v[138:139], s[12:13] op_sel_hi:[1,0]
	v_pk_add_f32 v[140:141], v[180:181], v[184:185]
	v_pk_fma_f32 v[88:89], v[88:89], v[152:153], v[148:149]
	v_pk_fma_f32 v[138:139], v[138:139], v[140:141], v[176:177]
	v_lshlrev_b32_e32 v140, 16, v78
	v_and_b32_e32 v141, 0xffff0000, v78
	v_cvt_pk_f32_fp8_sdwa v[148:149], v117 src0_sel:WORD_1
	v_cvt_pk_f32_fp8_sdwa v[152:153], v119 src0_sel:WORD_1
	s_waitcnt vmcnt(3)
	v_pk_mul_f32 v[84:85], v[84:85], s[12:13] op_sel_hi:[1,0]
	v_pk_add_f32 v[146:147], v[146:147], v[150:151]
	v_pk_mul_f32 v[130:131], v[130:131], s[12:13] op_sel_hi:[1,0]
	v_pk_fma_f32 v[84:85], v[84:85], v[146:147], v[140:141]
	v_cvt_pk_f32_fp8_e32 v[140:141], v116
	v_cvt_pk_f32_fp8_e32 v[146:147], v118
	v_cvt_pk_f32_fp8_sdwa v[116:117], v116 src0_sel:WORD_1
	v_cvt_pk_f32_fp8_sdwa v[118:119], v118 src0_sel:WORD_1
	v_pk_fma_f32 v[130:131], v[130:131], v[158:159], v[154:155]
	v_lshlrev_b32_e32 v78, 16, v79
	v_and_b32_e32 v79, 0xffff0000, v79
	v_pk_mul_f32 v[86:87], v[86:87], s[12:13] op_sel_hi:[1,0]
	v_pk_add_f32 v[148:149], v[148:149], v[152:153]
	v_mul_f32_e32 v43, v127, v127
	v_mul_f32_e32 v45, v131, v131
	v_pk_fma_f32 v[78:79], v[86:87], v[148:149], v[78:79]
	v_lshlrev_b32_e32 v86, 16, v76
	v_and_b32_e32 v87, 0xffff0000, v76
	s_waitcnt vmcnt(2)
; __device__ __forceinline__ float bf_lo(unsigned w) { return __uint_as_float(w << 16); }
; __device__ __forceinline__ float bf_hi(unsigned w) { return __uint_as_float(w & 0xffff0000u); }
; __device__ __forceinline__ void p9_final(const Params& P, int tid, int blk, int G) {
;     ...
;         for (int i = 0; i < 8; ++i) {
;             const int k = (i * 64 + lane) * 4;
;             const f32x4 xv = {bf_lo(xw[i].x), bf_hi(xw[i].x), bf_lo(xw[i].y), bf_hi(xw[i].y)};
;             const f32x4 gt = *(const f32x4*)(mod + (size_t)b * NMOD + 5 * DM + k) * (1.0f / Y2_SCALE);
;             const f32x2 a0 = __builtin_amdgcn_cvt_pk_f32_fp8((int)ya[i], false), a1 = __builtin_amdgcn_cvt_pk_f32_fp8((int)ya[i], true);
;             const f32x2 b0 = __builtin_amdgcn_cvt_pk_f32_fp8((int)yb[i], false), b1 = __builtin_amdgcn_cvt_pk_f32_fp8((int)yb[i], true);
;             const f32x4 y = {a0[0] + b0[0], a0[1] + b0[1], a1[0] + b1[0], a1[1] + b1[1]};
;             v[i] = xv + gt * y;
;             ss += v[i][0] * v[i][0] + v[i][1] * v[i][1] + v[i][2] * v[i][2] + v[i][3] * v[i][3];
;         }
;         ss = wave_sum(ss);
	v_pk_mul_f32 v[122:123], v[122:123], s[12:13] op_sel_hi:[1,0]
	v_pk_add_f32 v[140:141], v[140:141], v[146:147]
	v_pk_mul_f32 v[134:135], v[134:135], s[12:13] op_sel_hi:[1,0]
	v_pk_fma_f32 v[128:129], v[128:129], v[160:161], v[156:157]
	v_fmac_f32_e32 v43, v126, v126
	v_fmac_f32_e32 v45, v130, v130
	v_pk_fma_f32 v[86:87], v[122:123], v[140:141], v[86:87]
	v_pk_fma_f32 v[134:135], v[134:135], v[162:163], v[166:167]
	v_fmac_f32_e32 v43, v88, v88
	v_fmac_f32_e32 v45, v128, v128
	v_lshlrev_b32_e32 v76, 16, v77
	v_and_b32_e32 v77, 0xffff0000, v77
	v_pk_mul_f32 v[124:125], v[124:125], s[12:13] op_sel_hi:[1,0]
	v_pk_add_f32 v[116:117], v[116:117], v[118:119]
	v_mov_b32_e32 v118, v85
	v_mov_b32_e32 v119, v87
	v_mul_f32_e32 v47, v135, v135
	v_fmac_f32_e32 v43, v89, v89
	v_fmac_f32_e32 v45, v129, v129
	v_pk_fma_f32 v[76:77], v[124:125], v[116:117], v[76:77]
	v_mov_b32_e32 v116, v84
	v_mov_b32_e32 v117, v86
	v_pk_mul_f32 v[118:119], v[118:119], v[118:119]
	v_pk_fma_f32 v[132:133], v[132:133], v[164:165], v[168:169]
	v_fmac_f32_e32 v47, v134, v134
	v_add_f32_e32 v43, v43, v45
	v_mul_f32_e32 v45, v139, v139
	v_pk_fma_f32 v[116:117], v[116:117], v[116:117], v[118:119]
	v_mov_b32_e32 v118, v78
	v_mov_b32_e32 v119, v76
	v_fmac_f32_e32 v47, v132, v132
	v_fmac_f32_e32 v45, v138, v138
	v_pk_fma_f32 v[116:117], v[118:119], v[118:119], v[116:117]
	v_mov_b32_e32 v118, v79
	v_mov_b32_e32 v119, v77
	v_fmac_f32_e32 v47, v133, v133
	v_fmac_f32_e32 v45, v136, v136
	v_pk_fma_f32 v[116:117], v[118:119], v[118:119], v[116:117]
	v_cvt_pk_f32_fp8_e32 v[118:119], v114
	v_cvt_pk_f32_fp8_sdwa v[122:123], v114 src0_sel:WORD_1
	v_cvt_pk_f32_fp8_e32 v[124:125], v115
	v_cvt_pk_f32_fp8_sdwa v[114:115], v115 src0_sel:WORD_1
	v_add_f32_e32 v43, v43, v47
	v_fmac_f32_e32 v45, v137, v137
	v_add_f32_e32 v43, v43, v45
	v_add_f32_e32 v43, v43, v116
	v_add_f32_e32 v43, v43, v117
	v_lshlrev_b32_e32 v116, 16, v74
	v_and_b32_e32 v117, 0xffff0000, v74
	v_lshlrev_b32_e32 v74, 16, v75
	v_and_b32_e32 v75, 0xffff0000, v75
	s_waitcnt vmcnt(1)
	v_pk_mul_f32 v[82:83], v[82:83], s[12:13] op_sel_hi:[1,0]
	v_pk_mul_f32 v[80:81], v[80:81], s[12:13] op_sel_hi:[1,0]
	v_pk_add_f32 v[118:119], v[118:119], v[124:125]
	v_pk_add_f32 v[114:115], v[122:123], v[114:115]
	v_pk_fma_f32 v[80:81], v[80:81], v[118:119], v[116:117]
	v_pk_fma_f32 v[82:83], v[82:83], v[114:115], v[74:75]
	v_cvt_pk_f32_fp8_e32 v[114:115], v104
	v_cvt_pk_f32_fp8_e32 v[118:119], v113
	v_cvt_pk_f32_fp8_sdwa v[116:117], v104 src0_sel:WORD_1
	v_cvt_pk_f32_fp8_sdwa v[122:123], v113 src0_sel:WORD_1
	v_lshlrev_b32_e32 v74, 16, v72
	v_and_b32_e32 v75, 0xffff0000, v72
	s_waitcnt vmcnt(0)
	v_pk_mul_f32 v[140:141], v[142:143], s[12:13] op_sel_hi:[1,0]
	v_pk_add_f32 v[114:115], v[114:115], v[118:119]
	v_lshlrev_b32_e32 v72, 16, v73
	v_pk_fma_f32 v[114:115], v[140:141], v[114:115], v[74:75]
	v_and_b32_e32 v73, 0xffff0000, v73
	v_pk_mul_f32 v[124:125], v[144:145], s[12:13] op_sel_hi:[1,0]
	v_pk_add_f32 v[116:117], v[116:117], v[122:123]
	v_mov_b32_e32 v74, v81
	v_mov_b32_e32 v75, v115
	v_pk_fma_f32 v[116:117], v[124:125], v[116:117], v[72:73]
	v_mov_b32_e32 v72, v80
	v_mov_b32_e32 v73, v114
	v_pk_mul_f32 v[74:75], v[74:75], v[74:75]
	v_mov_b32_e32 v113, v105
	v_pk_fma_f32 v[72:73], v[72:73], v[72:73], v[74:75]
	v_mov_b32_e32 v74, v82
	v_mov_b32_e32 v75, v116
	v_pk_fma_f32 v[72:73], v[74:75], v[74:75], v[72:73]
	v_mov_b32_e32 v74, v83
	v_mov_b32_e32 v75, v117
	v_pk_fma_f32 v[72:73], v[74:75], v[74:75], v[72:73]
	v_mov_b32_e32 v118, v107
	v_add_f32_e32 v43, v43, v72
	v_add_f32_e32 v43, v43, v73
	ds_bpermute_b32 v45, v90, v43
	v_mov_b32_e32 v119, v108
	v_mov_b32_e32 v122, v110
	v_mov_b32_e32 v123, v111
	v_mov_b32_e32 v124, v112
	s_waitcnt lgkmcnt(0)
; __device__ __forceinline__ void p9_final(const Params& P, int tid, int blk, int G) {
;     ...
;         ss = wave_sum(ss);
;         const float r = rsqrtf(ss * (1.0f / 2048.0f) + 1e-6f);
;         float* xr = P.out + (size_t)row * DM;
; #pragma unroll
;         for (int i = 0; i < 8; ++i) { const int k = (i * 64 + lane) * 4; *(f32x4*)(xr + k) = v[i] * r * gf[i]; }
; #pragma unroll
;         for (int i = 0; i < 8; ++i) { xw[i] = xwn[i]; ya[i] = yan[i]; yb[i] = ybn[i]; }
	v_add_f32_e32 v43, v43, v45
	ds_bpermute_b32 v45, v91, v43
	s_waitcnt lgkmcnt(0)
	v_add_f32_e32 v43, v43, v45
	ds_bpermute_b32 v45, v92, v43
	s_waitcnt lgkmcnt(0)
	v_add_f32_e32 v43, v43, v45
	ds_bpermute_b32 v45, v93, v43
	s_waitcnt lgkmcnt(0)
	v_add_f32_e32 v43, v43, v45
	ds_bpermute_b32 v45, v94, v43
	s_waitcnt lgkmcnt(0)
	v_add_f32_e32 v43, v43, v45
	ds_bpermute_b32 v45, v95, v43
	s_waitcnt lgkmcnt(0)
	v_add_f32_e32 v43, v43, v45
	v_fmamk_f32 v43, v43, 0x3a000000, v96
	v_mul_f32_e32 v45, 0x4b800000, v43
	v_cmp_gt_f32_e64 s[0:1], s17, v43
	s_nop 1
	v_cndmask_b32_e64 v43, v43, v45, s[0:1]
	v_rsq_f32_e32 v43, v43
	s_nop 0
	v_mul_f32_e32 v45, 0x45800000, v43
	v_cndmask_b32_e64 v104, v43, v45, s[0:1]
	v_pk_mul_f32 v[72:73], v[126:127], v[104:105] op_sel_hi:[1,0]
	v_pk_mul_f32 v[74:75], v[88:89], v[104:105] op_sel_hi:[1,0]
	v_pk_mul_f32 v[72:73], v[2:3], v[72:73]
	v_pk_mul_f32 v[74:75], v[4:5], v[74:75]
	global_store_dwordx4 v[0:1], v[72:75], off offset:-4096 nt
	v_mov_b32_e32 v88, v120
	s_nop 0
	v_pk_mul_f32 v[72:73], v[130:131], v[104:105] op_sel_hi:[1,0]
	v_pk_mul_f32 v[74:75], v[128:129], v[104:105] op_sel_hi:[1,0]
	v_pk_mul_f32 v[72:73], v[6:7], v[72:73]
	v_pk_mul_f32 v[74:75], v[8:9], v[74:75]
	global_store_dwordx4 v[0:1], v[72:75], off offset:-3072 nt
	s_nop 1
	v_pk_mul_f32 v[72:73], v[134:135], v[104:105] op_sel_hi:[1,0]
	v_pk_mul_f32 v[74:75], v[132:133], v[104:105] op_sel_hi:[1,0]
	v_pk_mul_f32 v[72:73], v[10:11], v[72:73]
	v_pk_mul_f32 v[74:75], v[12:13], v[74:75]
	global_store_dwordx4 v[0:1], v[72:75], off offset:-2048 nt
	s_nop 1
	v_pk_mul_f32 v[72:73], v[138:139], v[104:105] op_sel_hi:[1,0]
	v_pk_mul_f32 v[74:75], v[136:137], v[104:105] op_sel_hi:[1,0]
	v_pk_mul_f32 v[72:73], v[14:15], v[72:73]
	v_pk_mul_f32 v[74:75], v[16:17], v[74:75]
	global_store_dwordx4 v[0:1], v[72:75], off offset:-1024 nt
	s_nop 1
	v_pk_mul_f32 v[72:73], v[84:85], v[104:105] op_sel_hi:[1,0]
	v_pk_mul_f32 v[74:75], v[78:79], v[104:105] op_sel_hi:[1,0]
	v_pk_mul_f32 v[72:73], v[18:19], v[72:73]
	v_pk_mul_f32 v[74:75], v[20:21], v[74:75]
	global_store_dwordx4 v[0:1], v[72:75], off nt
	v_mov_b32_e32 v84, v58
	v_mov_b32_e32 v85, v59
	v_pk_mul_f32 v[72:73], v[86:87], v[104:105] op_sel_hi:[1,0]
	v_pk_mul_f32 v[74:75], v[76:77], v[104:105] op_sel_hi:[1,0]
	v_pk_mul_f32 v[72:73], v[22:23], v[72:73]
	v_pk_mul_f32 v[74:75], v[24:25], v[74:75]
	global_store_dwordx4 v[0:1], v[72:75], off offset:1024 nt
	v_mov_b32_e32 v86, v56
	v_mov_b32_e32 v87, v57
	v_pk_mul_f32 v[72:73], v[80:81], v[104:105] op_sel_hi:[1,0]
	v_pk_mul_f32 v[74:75], v[82:83], v[104:105] op_sel_hi:[1,0]
	v_pk_mul_f32 v[72:73], v[26:27], v[72:73]
	v_pk_mul_f32 v[74:75], v[28:29], v[74:75]
	global_store_dwordx4 v[0:1], v[72:75], off offset:2048 nt
	v_mov_b32_e32 v82, v60
	v_mov_b32_e32 v83, v61
	v_pk_mul_f32 v[72:73], v[114:115], v[104:105] op_sel_hi:[1,0]
	v_pk_mul_f32 v[74:75], v[116:117], v[104:105] op_sel_hi:[1,0]
	v_pk_mul_f32 v[72:73], v[30:31], v[72:73]
	v_pk_mul_f32 v[74:75], v[32:33], v[74:75]
	global_store_dwordx4 v[0:1], v[72:75], off offset:3072 nt
	v_lshl_add_u64 v[0:1], v[0:1], 0, s[4:5]
	v_mov_b32_e32 v104, v39
	v_mov_b32_e32 v114, v97
	v_mov_b32_e32 v116, v98
	v_mov_b32_e32 v117, v99
	v_mov_b32_e32 v115, v106
	v_mov_b32_e32 v80, v62
	v_mov_b32_e32 v81, v63
	v_mov_b32_e32 v78, v64
	v_mov_b32_e32 v79, v65
	v_mov_b32_e32 v76, v66
	v_mov_b32_e32 v77, v67
	v_mov_b32_e32 v74, v68
	v_mov_b32_e32 v75, v69
	v_mov_b32_e32 v72, v70
	v_mov_b32_e32 v73, v71
	s_andn2_b64 exec, exec, s[8:9]
	s_cbranch_execz .LBB0_1462
